# baseline (speedup 1.0000x reference)
.LBB1_3:
	s_mov_b32 s29, s16
	v_add_u32_e32 v0, s29, v101
	ds_read_b128 v[94:97], v0 offset:16384
	ds_read_b128 v[102:105], v0 offset:17408
	ds_read_b128 v[106:109], v0 offset:18432
	ds_read_b128 v[110:113], v0 offset:19456
	ds_read_b128 v[114:117], v0 offset:32768
	ds_read_b128 v[118:121], v0 offset:33792
	ds_read_b128 v[122:125], v0 offset:34816
	ds_read_b128 v[126:129], v0 offset:35840
	s_lshl_b32 s16, s28, 2
	s_or_b32 s16, s16, s23
	s_lshl_b64 s[30:31], s[16:17], 19
	s_add_u32 s16, s6, s30
	s_addc_u32 s31, s7, s31
	s_lshl_b32 s33, s3, 7
	s_ashr_i32 s35, s33, 31
	s_add_u32 s30, s16, s33
	s_addc_u32 s31, s31, s35
	s_add_u32 s34, s4, s33
	s_addc_u32 s35, s5, s35
	s_add_i32 s16, s19, s27
	s_add_i32 m0, s16, 0x4000
	v_add_u32_e32 v0, s29, v91
	global_load_lds_dwordx4 v84, s[30:31]
	ds_read_b128 v[130:133], v0
	ds_read_b128 v[134:137], v0 offset:1024
	s_add_i32 m0, s16, 0x6000
	ds_read_b128 v[138:141], v0 offset:2048
	global_load_lds_dwordx4 v88, s[30:31]
	ds_read_b128 v[142:145], v0 offset:3072
	ds_read_b128 v[146:149], v0 offset:4096
	s_mov_b32 m0, s16
	ds_read_b128 v[150:153], v0 offset:5120
	global_load_lds_dwordx4 v82, s[34:35]
	ds_read_b128 v[154:157], v0 offset:6144
	ds_read_b128 v[158:161], v0 offset:7168
	s_waitcnt vmcnt(3) lgkmcnt(0)
	s_barrier
	s_setprio 1
	v_mfma_f32_16x16x32_f16 v[78:81], v[94:97], v[130:133], v[78:81]
	s_add_u32 s30, s30, 0x40000
	s_addc_u32 s31, s31, 0
	s_add_i32 m0, s16, 0x8000
	v_mfma_f32_16x16x32_f16 v[74:77], v[106:109], v[130:133], v[74:77]
	global_load_lds_dwordx4 v84, s[30:31]
	s_add_i32 m0, s16, 0xa000
	v_mfma_f32_16x16x32_f16 v[66:69], v[94:97], v[138:141], v[66:69]
	global_load_lds_dwordx4 v88, s[30:31]
	s_add_i32 m0, s16, 0x2000
	v_mfma_f32_16x16x32_f16 v[58:61], v[106:109], v[138:141], v[58:61]
	global_load_lds_dwordx4 v86, s[34:35]
	v_mfma_f32_16x16x32_f16 v[78:81], v[102:105], v[134:137], v[78:81]
	v_mfma_f32_16x16x32_f16 v[74:77], v[110:113], v[134:137], v[74:77]
	v_mfma_f32_16x16x32_f16 v[66:69], v[102:105], v[142:145], v[66:69]
	v_mfma_f32_16x16x32_f16 v[58:61], v[110:113], v[142:145], v[58:61]
	v_mfma_f32_16x16x32_f16 v[54:57], v[94:97], v[146:149], v[54:57]
	v_mfma_f32_16x16x32_f16 v[46:49], v[106:109], v[146:149], v[46:49]
	v_mfma_f32_16x16x32_f16 v[34:37], v[94:97], v[154:157], v[34:37]
	v_mfma_f32_16x16x32_f16 v[26:29], v[106:109], v[154:157], v[26:29]
	v_mfma_f32_16x16x32_f16 v[54:57], v[102:105], v[150:153], v[54:57]
	v_mfma_f32_16x16x32_f16 v[46:49], v[110:113], v[150:153], v[46:49]
	v_mfma_f32_16x16x32_f16 v[34:37], v[102:105], v[158:161], v[34:37]
	v_mfma_f32_16x16x32_f16 v[26:29], v[110:113], v[158:161], v[26:29]
	v_mfma_f32_16x16x32_f16 v[70:73], v[114:117], v[130:133], v[70:73]
	v_mfma_f32_16x16x32_f16 v[62:65], v[122:125], v[130:133], v[62:65]
	v_mfma_f32_16x16x32_f16 v[50:53], v[114:117], v[138:141], v[50:53]
	v_mfma_f32_16x16x32_f16 v[42:45], v[122:125], v[138:141], v[42:45]
	v_mfma_f32_16x16x32_f16 v[70:73], v[118:121], v[134:137], v[70:73]
	v_mfma_f32_16x16x32_f16 v[62:65], v[126:129], v[134:137], v[62:65]
	v_mfma_f32_16x16x32_f16 v[50:53], v[118:121], v[142:145], v[50:53]
	v_mfma_f32_16x16x32_f16 v[42:45], v[126:129], v[142:145], v[42:45]
	v_mfma_f32_16x16x32_f16 v[38:41], v[114:117], v[146:149], v[38:41]
	v_mfma_f32_16x16x32_f16 v[30:33], v[122:125], v[146:149], v[30:33]
	s_add_i32 s3, s3, 1
	s_bitcmp1_b32 s3, 4
	s_addc_u32 s28, s28, 0
	v_mfma_f32_16x16x32_f16 v[22:25], v[114:117], v[154:157], v[22:25]
	s_and_b32 s3, s3, 15
	v_mfma_f32_16x16x32_f16 v[2:5], v[122:125], v[154:157], v[2:5]
	v_mfma_f32_16x16x32_f16 v[38:41], v[118:121], v[150:153], v[38:41]
	v_mfma_f32_16x16x32_f16 v[30:33], v[126:129], v[150:153], v[30:33]
	s_add_i32 s26, s26, -1
	v_mfma_f32_16x16x32_f16 v[22:25], v[118:121], v[158:161], v[22:25]
	s_mov_b32 s16, s24
	s_mov_b32 s24, s27
	v_mfma_f32_16x16x32_f16 v[2:5], v[126:129], v[158:161], v[2:5]
	s_mov_b32 s27, s29
	s_cmp_lg_u32 s26, 0
	s_setprio 0
	s_barrier
	s_cbranch_scc1 .LBB1_3
	s_lshl_b32 s3, s14, 7
	s_add_i32 s17, s25, s3
	s_ashr_i32 s3, s17, 1
	s_lshr_b32 s14, s17, 5
	s_or_b32 s24, s15, s2
	s_and_b32 s14, s14, 62
	s_and_b32 s27, s3, 0xfffffc00
	v_or_b32_e32 v105, s24, v1
	v_lshlrev_b32_e32 v98, 4, v93
	v_or_b32_e32 v102, 16, v93
	v_or_b32_e32 v103, 32, v93
	v_or_b32_e32 v104, 48, v93
	v_mov_b32_e32 v93, 0
	s_and_b32 s16, s24, 0x340
	v_lshlrev_b32_e32 v95, 6, v105
	s_or_b32 s2, s27, s14
	v_lshlrev_b32_e32 v0, 9, v92
	v_and_b32_e32 v110, 0xc00, v95
	v_mov_b32_e32 v111, v93
	s_or_b32 s14, s2, s16
	v_and_b32_e32 v92, 0x200, v0
	v_lshl_add_u64 v[110:111], s[8:9], 0, v[110:111]
	s_or_b32 s30, s14, 0x80
	s_mov_b32 s3, 0
	v_mov_b32_e32 v99, v93
	v_lshl_add_u64 v[110:111], v[110:111], 0, v[92:93]
	s_mov_b32 s2, 0x3e38aa3b
	v_pk_add_f32 v[72:73], v[12:13], v[72:73]
	v_pk_add_f32 v[70:71], v[10:11], v[70:71]
	v_pk_add_f32 v[64:65], v[8:9], v[64:65]
	v_pk_add_f32 v[62:63], v[6:7], v[62:63]
	s_ashr_i32 s31, s30, 31
	v_lshl_add_u64 v[112:113], v[110:111], 0, v[98:99]
	v_pk_mul_f32 v[72:73], v[72:73], s[2:3] op_sel_hi:[1,0]
	v_pk_mul_f32 v[70:71], v[70:71], s[2:3] op_sel_hi:[1,0]
	v_pk_mul_f32 v[64:65], v[64:65], s[2:3] op_sel_hi:[1,0]
	v_pk_mul_f32 v[62:63], v[62:63], s[2:3] op_sel_hi:[1,0]
	s_lshl_b64 s[30:31], s[30:31], 12
	v_lshlrev_b32_e32 v96, 4, v102
	v_mov_b32_e32 v97, v93
	v_pk_add_f32 v[80:81], v[20:21], v[80:81]
	v_pk_add_f32 v[78:79], v[18:19], v[78:79]
	v_pk_add_f32 v[74:75], v[14:15], v[74:75]
	s_ashr_i32 s15, s14, 31
	v_cvt_pk_f16_f32 v70, v70, v71
	v_cvt_pk_f16_f32 v71, v72, v73
	v_cvt_pk_f16_f32 v72, v62, v63
	v_cvt_pk_f16_f32 v73, v64, v65
	v_lshl_add_u64 v[62:63], v[112:113], 0, s[30:31]
	v_pk_add_f32 v[58:59], v[14:15], v[58:59]
	v_pk_mul_f32 v[80:81], v[80:81], s[2:3] op_sel_hi:[1,0]
	v_pk_mul_f32 v[78:79], v[78:79], s[2:3] op_sel_hi:[1,0]
	v_pk_mul_f32 v[74:75], v[74:75], s[2:3] op_sel_hi:[1,0]
	s_lshl_b64 s[28:29], s[14:15], 12
	global_store_dwordx4 v[62:63], v[70:73], off
	v_pk_add_f32 v[62:63], v[20:21], v[68:69]
	v_pk_add_f32 v[64:65], v[18:19], v[66:67]
	v_lshl_add_u64 v[70:71], v[110:111], 0, v[96:97]
	v_pk_mul_f32 v[58:59], v[58:59], s[2:3] op_sel_hi:[1,0]
	v_pk_add_f32 v[52:53], v[12:13], v[52:53]
	v_pk_add_f32 v[50:51], v[10:11], v[50:51]
	v_pk_add_f32 v[44:45], v[8:9], v[44:45]
	v_pk_add_f32 v[42:43], v[6:7], v[42:43]
	v_lshlrev_b32_e32 v0, 4, v103
	v_cvt_pk_f16_f32 v78, v78, v79
	v_cvt_pk_f16_f32 v79, v80, v81
	v_cvt_pk_f16_f32 v80, v74, v75
	v_lshl_add_u64 v[74:75], v[112:113], 0, s[28:29]
	v_pk_mul_f32 v[66:67], v[62:63], s[2:3] op_sel_hi:[1,0]
	v_pk_mul_f32 v[62:63], v[64:65], s[2:3] op_sel_hi:[1,0]
	v_cvt_pk_f16_f32 v64, v58, v59
	v_lshl_add_u64 v[58:59], v[70:71], 0, s[28:29]
	v_pk_mul_f32 v[52:53], v[52:53], s[2:3] op_sel_hi:[1,0]
	v_pk_mul_f32 v[50:51], v[50:51], s[2:3] op_sel_hi:[1,0]
	v_pk_mul_f32 v[44:45], v[44:45], s[2:3] op_sel_hi:[1,0]
	v_pk_mul_f32 v[42:43], v[42:43], s[2:3] op_sel_hi:[1,0]
	s_or_b32 s28, s14, 1
	s_or_b32 s14, s14, 0x81
	v_and_b32_e32 v106, 0xf0, v0
	v_mov_b32_e32 v107, v93
	v_cvt_pk_f16_f32 v50, v50, v51
	v_cvt_pk_f16_f32 v51, v52, v53
	v_cvt_pk_f16_f32 v52, v42, v43
	v_cvt_pk_f16_f32 v53, v44, v45
	v_lshl_add_u64 v[42:43], v[70:71], 0, s[30:31]
	v_pk_add_f32 v[40:41], v[12:13], v[40:41]
	v_pk_add_f32 v[38:39], v[10:11], v[38:39]
	v_pk_add_f32 v[32:33], v[8:9], v[32:33]
	v_pk_add_f32 v[30:31], v[6:7], v[30:31]
	s_ashr_i32 s15, s14, 31
	v_lshlrev_b32_e32 v94, 4, v104
	global_store_dwordx4 v[42:43], v[50:53], off
	v_pk_mul_f32 v[40:41], v[40:41], s[2:3] op_sel_hi:[1,0]
	v_pk_mul_f32 v[38:39], v[38:39], s[2:3] op_sel_hi:[1,0]
	v_lshl_add_u64 v[50:51], v[110:111], 0, v[106:107]
	v_pk_mul_f32 v[32:33], v[32:33], s[2:3] op_sel_hi:[1,0]
	v_pk_mul_f32 v[30:31], v[30:31], s[2:3] op_sel_hi:[1,0]
	s_lshl_b64 s[14:15], s[14:15], 12
	v_and_b32_e32 v108, 0x1f0, v94
	v_mov_b32_e32 v109, v93
	v_pk_add_f32 v[42:43], v[20:21], v[56:57]
	v_pk_add_f32 v[44:45], v[18:19], v[54:55]
	v_pk_add_f32 v[46:47], v[14:15], v[46:47]
	s_ashr_i32 s29, s28, 31
	v_cvt_pk_f16_f32 v38, v38, v39
	v_cvt_pk_f16_f32 v39, v40, v41
	v_cvt_pk_f16_f32 v40, v30, v31
	v_cvt_pk_f16_f32 v41, v32, v33
	v_lshl_add_u64 v[30:31], v[50:51], 0, s[14:15]
	v_pk_add_f32 v[20:21], v[20:21], v[36:37]
	v_pk_add_f32 v[18:19], v[18:19], v[34:35]
	v_pk_add_f32 v[14:15], v[14:15], v[26:27]
	v_pk_add_f32 v[76:77], v[16:17], v[76:77]
	v_pk_add_f32 v[60:61], v[16:17], v[60:61]
	v_pk_mul_f32 v[52:53], v[42:43], s[2:3] op_sel_hi:[1,0]
	v_pk_mul_f32 v[42:43], v[44:45], s[2:3] op_sel_hi:[1,0]
	v_pk_add_f32 v[44:45], v[16:17], v[48:49]
	s_lshl_b64 s[28:29], s[28:29], 12
	global_store_dwordx4 v[30:31], v[38:41], off
	v_lshl_add_u64 v[30:31], v[110:111], 0, v[108:109]
	v_pk_mul_f32 v[20:21], v[20:21], s[2:3] op_sel_hi:[1,0]
	v_pk_mul_f32 v[18:19], v[18:19], s[2:3] op_sel_hi:[1,0]
	v_pk_add_f32 v[16:17], v[16:17], v[28:29]
	v_pk_mul_f32 v[14:15], v[14:15], s[2:3] op_sel_hi:[1,0]
	v_pk_add_f32 v[12:13], v[12:13], v[24:25]
	v_pk_add_f32 v[10:11], v[10:11], v[22:23]
	v_pk_add_f32 v[4:5], v[8:9], v[4:5]
	v_pk_add_f32 v[2:3], v[6:7], v[2:3]
	v_pk_mul_f32 v[76:77], v[76:77], s[2:3] op_sel_hi:[1,0]
	v_pk_mul_f32 v[60:61], v[60:61], s[2:3] op_sel_hi:[1,0]
	v_pk_mul_f32 v[48:49], v[44:45], s[2:3] op_sel_hi:[1,0]
	v_pk_mul_f32 v[44:45], v[46:47], s[2:3] op_sel_hi:[1,0]
	v_lshl_add_u64 v[46:47], v[50:51], 0, s[28:29]
	v_cvt_pk_f16_f32 v18, v18, v19
	v_cvt_pk_f16_f32 v19, v20, v21
	v_pk_mul_f32 v[16:17], v[16:17], s[2:3] op_sel_hi:[1,0]
	v_cvt_pk_f16_f32 v20, v14, v15
	v_lshl_add_u64 v[14:15], v[30:31], 0, s[28:29]
	v_pk_mul_f32 v[12:13], v[12:13], s[2:3] op_sel_hi:[1,0]
	v_pk_mul_f32 v[10:11], v[10:11], s[2:3] op_sel_hi:[1,0]
	v_pk_mul_f32 v[4:5], v[4:5], s[2:3] op_sel_hi:[1,0]
	v_pk_mul_f32 v[2:3], v[2:3], s[2:3] op_sel_hi:[1,0]
	s_add_u32 s28, s20, s22
	v_cvt_pk_f16_f32 v81, v76, v77
	v_cvt_pk_f16_f32 v62, v62, v63
	v_cvt_pk_f16_f32 v63, v66, v67
	v_cvt_pk_f16_f32 v65, v60, v61
	v_cvt_pk_f16_f32 v42, v42, v43
	v_cvt_pk_f16_f32 v43, v52, v53
	v_cvt_pk_f16_f32 v44, v44, v45
	v_cvt_pk_f16_f32 v45, v48, v49
	v_cvt_pk_f16_f32 v21, v16, v17
	v_cvt_pk_f16_f32 v10, v10, v11
	v_cvt_pk_f16_f32 v11, v12, v13
	v_cvt_pk_f16_f32 v12, v2, v3
	v_cvt_pk_f16_f32 v13, v4, v5
	v_lshl_add_u64 v[2:3], v[30:31], 0, s[14:15]
	s_addc_u32 s29, s21, 0
	v_lshlrev_b32_e32 v92, 2, v1
	global_store_dwordx4 v[74:75], v[78:81], off
	global_store_dwordx4 v[58:59], v[62:65], off
	global_store_dwordx4 v[46:47], v[42:45], off
	global_store_dwordx4 v[14:15], v[18:21], off
	global_store_dwordx4 v[2:3], v[10:13], off
	v_lshl_add_u64 v[2:3], s[28:29], 0, v[92:93]
	s_mov_b64 s[28:29], 0x1000
	v_lshl_add_u64 v[10:11], v[2:3], 0, s[28:29]
	global_load_dwordx4 v[22:25], v[10:11], off
	global_load_dwordx4 v[14:17], v[10:11], off offset:16
	global_load_dwordx4 v[6:9], v[10:11], off offset:512
	global_load_dwordx4 v[2:5], v[10:11], off offset:528
	s_mov_b32 s25, 1
	s_mov_b32 s26, 16
	s_mov_b32 s14, 2
	s_mov_b32 s15, 0x18000
	s_mov_b32 s2, 0xc000
	s_mov_b32 s27, 0
	v_mov_b32_e32 v10, v93
	v_mov_b32_e32 v11, v93
	v_mov_b32_e32 v12, v93
	v_mov_b32_e32 v13, v93
	v_mov_b32_e32 v18, v93
	v_mov_b32_e32 v19, v93
	v_mov_b32_e32 v20, v93
	v_mov_b32_e32 v21, v93
	v_mov_b32_e32 v26, v93
	v_mov_b32_e32 v27, v93
	v_mov_b32_e32 v28, v93
	v_mov_b32_e32 v29, v93
	v_mov_b32_e32 v34, v93
	v_mov_b32_e32 v35, v93
	v_mov_b32_e32 v36, v93
	v_mov_b32_e32 v37, v93
	v_mov_b32_e32 v42, v93
	v_mov_b32_e32 v43, v93
	v_mov_b32_e32 v44, v93
	v_mov_b32_e32 v45, v93
	v_mov_b32_e32 v50, v93
	v_mov_b32_e32 v51, v93
	v_mov_b32_e32 v52, v93
	v_mov_b32_e32 v53, v93
	v_mov_b32_e32 v62, v93
	v_mov_b32_e32 v63, v93
	v_mov_b32_e32 v64, v93
	v_mov_b32_e32 v65, v93
	v_mov_b32_e32 v70, v93
	v_mov_b32_e32 v71, v93
	v_mov_b32_e32 v72, v93
	v_mov_b32_e32 v73, v93
	v_mov_b32_e32 v30, v93
	v_mov_b32_e32 v31, v93
	v_mov_b32_e32 v32, v93
	v_mov_b32_e32 v33, v93
	v_mov_b32_e32 v38, v93
	v_mov_b32_e32 v39, v93
	v_mov_b32_e32 v40, v93
	v_mov_b32_e32 v41, v93
	v_mov_b32_e32 v46, v93
	v_mov_b32_e32 v47, v93
	v_mov_b32_e32 v48, v93
	v_mov_b32_e32 v49, v93
	v_mov_b32_e32 v54, v93
	v_mov_b32_e32 v55, v93
	v_mov_b32_e32 v56, v93
	v_mov_b32_e32 v57, v93
	v_mov_b32_e32 v58, v93
	v_mov_b32_e32 v59, v93
	v_mov_b32_e32 v60, v93
	v_mov_b32_e32 v61, v93
	v_mov_b32_e32 v66, v93
	v_mov_b32_e32 v67, v93
	v_mov_b32_e32 v68, v93
	v_mov_b32_e32 v69, v93
	v_mov_b32_e32 v74, v93
	v_mov_b32_e32 v75, v93
	v_mov_b32_e32 v76, v93
	v_mov_b32_e32 v77, v93
	v_mov_b32_e32 v78, v93
	v_mov_b32_e32 v79, v93
	v_mov_b32_e32 v80, v93
	v_mov_b32_e32 v81, v93
.LBB1_5:
	s_mov_b32 s28, s2
	v_add_u32_e32 v1, s28, v101
	ds_read_b128 v[106:109], v1 offset:16384
	ds_read_b128 v[110:113], v1 offset:17408
	ds_read_b128 v[114:117], v1 offset:18432
	ds_read_b128 v[118:121], v1 offset:19456
	ds_read_b128 v[122:125], v1 offset:32768
	ds_read_b128 v[126:129], v1 offset:33792
	ds_read_b128 v[130:133], v1 offset:34816
	ds_read_b128 v[134:137], v1 offset:35840
	s_lshl_b32 s2, s25, 2
	s_or_b32 s2, s2, s23
	s_lshl_b64 s[30:31], s[2:3], 19
	s_add_u32 s2, s6, s30
	s_addc_u32 s29, s7, s31
	s_lshl_b32 s33, s14, 7
	s_ashr_i32 s35, s33, 31
	s_add_u32 s30, s2, s33
	s_addc_u32 s31, s29, s35
	s_add_u32 s34, s4, s33
	s_addc_u32 s35, s5, s35
	s_add_i32 s2, s19, s27
	s_add_i32 m0, s2, 0x4000
	v_add_u32_e32 v1, s28, v91
	global_load_lds_dwordx4 v84, s[30:31]
	ds_read_b128 v[138:141], v1
	ds_read_b128 v[142:145], v1 offset:1024
	s_add_i32 m0, s2, 0x6000
	ds_read_b128 v[146:149], v1 offset:2048
	global_load_lds_dwordx4 v88, s[30:31]
	ds_read_b128 v[150:153], v1 offset:3072
	ds_read_b128 v[154:157], v1 offset:4096
	s_mov_b32 m0, s2
	ds_read_b128 v[158:161], v1 offset:5120
	global_load_lds_dwordx4 v82, s[34:35]
	ds_read_b128 v[162:165], v1 offset:6144
	ds_read_b128 v[166:169], v1 offset:7168
	s_waitcnt vmcnt(3) lgkmcnt(0)
	s_barrier
	s_setprio 1
	v_mfma_f32_16x16x32_f16 v[78:81], v[106:109], v[138:141], v[78:81]
	s_add_u32 s30, s30, 0x40000
	s_addc_u32 s31, s31, 0
	s_add_i32 m0, s2, 0x8000
	v_mfma_f32_16x16x32_f16 v[74:77], v[114:117], v[138:141], v[74:77]
	global_load_lds_dwordx4 v84, s[30:31]
	s_add_i32 m0, s2, 0xa000
	v_mfma_f32_16x16x32_f16 v[66:69], v[106:109], v[146:149], v[66:69]
	global_load_lds_dwordx4 v88, s[30:31]
	s_add_i32 m0, s2, 0x2000
	v_mfma_f32_16x16x32_f16 v[58:61], v[114:117], v[146:149], v[58:61]
	global_load_lds_dwordx4 v86, s[34:35]
	v_mfma_f32_16x16x32_f16 v[78:81], v[110:113], v[142:145], v[78:81]
	v_mfma_f32_16x16x32_f16 v[74:77], v[118:121], v[142:145], v[74:77]
	v_mfma_f32_16x16x32_f16 v[66:69], v[110:113], v[150:153], v[66:69]
	v_mfma_f32_16x16x32_f16 v[58:61], v[118:121], v[150:153], v[58:61]
	v_mfma_f32_16x16x32_f16 v[54:57], v[106:109], v[154:157], v[54:57]
	v_mfma_f32_16x16x32_f16 v[46:49], v[114:117], v[154:157], v[46:49]
	v_mfma_f32_16x16x32_f16 v[38:41], v[106:109], v[162:165], v[38:41]
	v_mfma_f32_16x16x32_f16 v[30:33], v[114:117], v[162:165], v[30:33]
	v_mfma_f32_16x16x32_f16 v[54:57], v[110:113], v[158:161], v[54:57]
	v_mfma_f32_16x16x32_f16 v[46:49], v[118:121], v[158:161], v[46:49]
	v_mfma_f32_16x16x32_f16 v[38:41], v[110:113], v[166:169], v[38:41]
	v_mfma_f32_16x16x32_f16 v[30:33], v[118:121], v[166:169], v[30:33]
	v_mfma_f32_16x16x32_f16 v[70:73], v[122:125], v[138:141], v[70:73]
	v_mfma_f32_16x16x32_f16 v[62:65], v[130:133], v[138:141], v[62:65]
	v_mfma_f32_16x16x32_f16 v[50:53], v[122:125], v[146:149], v[50:53]
	v_mfma_f32_16x16x32_f16 v[42:45], v[130:133], v[146:149], v[42:45]
	v_mfma_f32_16x16x32_f16 v[70:73], v[126:129], v[142:145], v[70:73]
	v_mfma_f32_16x16x32_f16 v[62:65], v[134:137], v[142:145], v[62:65]
	v_mfma_f32_16x16x32_f16 v[50:53], v[126:129], v[150:153], v[50:53]
	v_mfma_f32_16x16x32_f16 v[42:45], v[134:137], v[150:153], v[42:45]
	v_mfma_f32_16x16x32_f16 v[34:37], v[122:125], v[154:157], v[34:37]
	v_mfma_f32_16x16x32_f16 v[26:29], v[130:133], v[154:157], v[26:29]
	s_add_i32 s14, s14, 1
	s_bitcmp1_b32 s14, 4
	s_addc_u32 s25, s25, 0
	v_mfma_f32_16x16x32_f16 v[18:21], v[122:125], v[162:165], v[18:21]
	s_and_b32 s14, s14, 15
	v_mfma_f32_16x16x32_f16 v[10:13], v[130:133], v[162:165], v[10:13]
	v_mfma_f32_16x16x32_f16 v[34:37], v[126:129], v[158:161], v[34:37]
	v_mfma_f32_16x16x32_f16 v[26:29], v[134:137], v[158:161], v[26:29]
	s_add_i32 s26, s26, -1
	v_mfma_f32_16x16x32_f16 v[18:21], v[126:129], v[166:169], v[18:21]
	s_mov_b32 s2, s15
	s_mov_b32 s15, s27
	v_mfma_f32_16x16x32_f16 v[10:13], v[134:137], v[166:169], v[10:13]
	s_mov_b32 s27, s28
	s_cmp_lg_u32 s26, 0
	s_setprio 0
	s_barrier
	s_cbranch_scc1 .LBB1_5
	s_ashr_i32 s2, s17, 7
	s_and_b32 s3, s2, -16
	s_or_b32 s2, s3, 2
	s_sub_u32 s14, s10, s8
	s_subb_u32 s11, s11, s9
	s_bfe_u32 s6, s17, 0x50006
	s_add_u32 s14, s8, s14
	s_addc_u32 s15, s9, s11
	s_lshr_b32 s11, s24, 6
	s_or_b32 s17, s11, s3
	s_lshl_b32 s17, s17, 8
	s_lshl_b32 s23, s6, 3
	v_bfe_u32 v93, v105, 3, 3
	v_pk_add_f32 v[80:81], v[24:25], v[80:81]
	v_pk_add_f32 v[78:79], v[22:23], v[78:79]
	v_pk_add_f32 v[74:75], v[14:15], v[74:75]
	s_or_b32 s17, s17, s23
	s_or_b32 s11, s2, s11
	v_cvt_pk_f16_f32 v78, v78, v79
	v_cvt_pk_f16_f32 v79, v80, v81
	v_cvt_pk_f16_f32 v80, v74, v75
	v_or_b32_e32 v74, s17, v93
	s_lshl_b32 s11, s11, 8
	v_ashrrev_i32_e32 v75, 31, v74
	v_pk_add_f32 v[72:73], v[8:9], v[72:73]
	v_pk_add_f32 v[70:71], v[6:7], v[70:71]
	v_pk_add_f32 v[62:63], v[2:3], v[62:63]
	s_or_b32 s11, s11, s23
	v_lshlrev_b64 v[74:75], 10, v[74:75]
	v_cvt_pk_f16_f32 v70, v70, v71
	v_cvt_pk_f16_f32 v71, v72, v73
	v_cvt_pk_f16_f32 v72, v62, v63
	v_or_b32_e32 v62, s11, v93
	v_pk_add_f32 v[76:77], v[16:17], v[76:77]
	v_lshl_add_u64 v[74:75], s[14:15], 0, v[74:75]
	v_ashrrev_i32_e32 v63, 31, v62
	v_cvt_pk_f16_f32 v81, v76, v77
	v_lshl_add_u64 v[76:77], v[74:75], 0, v[98:99]
	v_lshlrev_b64 v[62:63], 10, v[62:63]
	global_store_dwordx4 v[76:77], v[78:81], off
	v_pk_add_f32 v[64:65], v[4:5], v[64:65]
	v_lshl_add_u64 v[76:77], s[14:15], 0, v[62:63]
	v_cvt_pk_f16_f32 v73, v64, v65
	v_lshl_add_u64 v[62:63], v[76:77], 0, v[98:99]
	global_store_dwordx4 v[62:63], v[70:73], off
	v_pk_add_f32 v[64:65], v[24:25], v[68:69]
	v_pk_add_f32 v[62:63], v[22:23], v[66:67]
	v_pk_add_f32 v[60:61], v[16:17], v[60:61]
	v_pk_add_f32 v[58:59], v[14:15], v[58:59]
	v_pk_add_f32 v[52:53], v[8:9], v[52:53]
	v_pk_add_f32 v[50:51], v[6:7], v[50:51]
	v_pk_add_f32 v[44:45], v[4:5], v[44:45]
	v_pk_add_f32 v[42:43], v[2:3], v[42:43]
	v_cvt_pk_f16_f32 v62, v62, v63
	v_cvt_pk_f16_f32 v63, v64, v65
	v_cvt_pk_f16_f32 v64, v58, v59
	v_cvt_pk_f16_f32 v65, v60, v61
	v_lshl_add_u64 v[58:59], v[74:75], 0, v[96:97]
	v_cvt_pk_f16_f32 v50, v50, v51
	v_cvt_pk_f16_f32 v51, v52, v53
	v_cvt_pk_f16_f32 v52, v42, v43
	v_cvt_pk_f16_f32 v53, v44, v45
	v_lshl_add_u64 v[42:43], v[76:77], 0, v[96:97]
	v_mov_b32_e32 v1, 0
	global_store_dwordx4 v[58:59], v[62:65], off
	global_store_dwordx4 v[42:43], v[50:53], off
	v_pk_add_f32 v[44:45], v[24:25], v[56:57]
	v_pk_add_f32 v[42:43], v[22:23], v[54:55]
	v_mov_b32_e32 v95, v1
	v_cvt_pk_f16_f32 v42, v42, v43
	v_cvt_pk_f16_f32 v43, v44, v45
	v_pk_add_f32 v[48:49], v[16:17], v[48:49]
	v_pk_add_f32 v[44:45], v[14:15], v[46:47]
	v_pk_add_f32 v[36:37], v[8:9], v[36:37]
	v_pk_add_f32 v[34:35], v[6:7], v[34:35]
	v_pk_add_f32 v[28:29], v[4:5], v[28:29]
	v_pk_add_f32 v[26:27], v[2:3], v[26:27]
	v_pk_add_f32 v[24:25], v[24:25], v[40:41]
	v_pk_add_f32 v[22:23], v[22:23], v[38:39]
	v_pk_add_f32 v[16:17], v[16:17], v[32:33]
	v_pk_add_f32 v[14:15], v[14:15], v[30:31]
	v_pk_add_f32 v[8:9], v[8:9], v[20:21]
	v_pk_add_f32 v[6:7], v[6:7], v[18:19]
	v_pk_add_f32 v[4:5], v[4:5], v[12:13]
	v_pk_add_f32 v[2:3], v[2:3], v[10:11]
	s_add_u32 s14, s20, s22
	v_cvt_pk_f16_f32 v44, v44, v45
	v_cvt_pk_f16_f32 v45, v48, v49
	v_lshl_add_u64 v[46:47], v[74:75], 0, v[0:1]
	v_cvt_pk_f16_f32 v34, v34, v35
	v_cvt_pk_f16_f32 v35, v36, v37
	v_cvt_pk_f16_f32 v36, v26, v27
	v_cvt_pk_f16_f32 v37, v28, v29
	v_lshl_add_u64 v[26:27], v[76:77], 0, v[0:1]
	v_cvt_pk_f16_f32 v22, v22, v23
	v_cvt_pk_f16_f32 v23, v24, v25
	v_cvt_pk_f16_f32 v24, v14, v15
	v_cvt_pk_f16_f32 v25, v16, v17
	v_lshl_add_u64 v[14:15], v[74:75], 0, v[94:95]
	v_cvt_pk_f16_f32 v6, v6, v7
	v_cvt_pk_f16_f32 v7, v8, v9
	v_cvt_pk_f16_f32 v8, v2, v3
	v_cvt_pk_f16_f32 v9, v4, v5
	v_lshl_add_u64 v[2:3], v[76:77], 0, v[94:95]
	s_addc_u32 s15, s21, 0
	v_mov_b32_e32 v93, v1
	global_store_dwordx4 v[46:47], v[42:45], off
	global_store_dwordx4 v[26:27], v[34:37], off
	global_store_dwordx4 v[14:15], v[22:25], off
	global_store_dwordx4 v[2:3], v[6:9], off
	v_lshl_add_u64 v[2:3], s[14:15], 0, v[92:93]
	s_mov_b64 s[14:15], 0x2000
	v_lshl_add_u64 v[2:3], v[2:3], 0, s[14:15]
	global_load_dwordx4 v[20:23], v[2:3], off
	global_load_dwordx4 v[12:15], v[2:3], off offset:16
	global_load_dwordx4 v[8:11], v[2:3], off offset:512
	global_load_dwordx4 v[4:7], v[2:3], off offset:528
	s_add_u32 s11, s12, 0x400000
	s_mov_b32 s7, 2
	v_and_b32_e32 v106, 56, v105
	s_mov_b32 s10, 0
	s_addc_u32 s12, s13, 0
	s_mov_b32 s14, 0xc000
	s_mov_b32 s17, 0x18000
	s_mov_b32 s13, 16
	v_mov_b32_e32 v0, v1
	v_mov_b32_e32 v2, v1
	v_mov_b32_e32 v3, v1
	v_mov_b32_e32 v16, v1
	v_mov_b32_e32 v17, v1
	v_mov_b32_e32 v18, v1
	v_mov_b32_e32 v19, v1
	v_mov_b32_e32 v24, v1
	v_mov_b32_e32 v25, v1
	v_mov_b32_e32 v26, v1
	v_mov_b32_e32 v27, v1
	v_mov_b32_e32 v32, v1
	v_mov_b32_e32 v33, v1
	v_mov_b32_e32 v34, v1
	v_mov_b32_e32 v35, v1
	v_mov_b32_e32 v40, v1
	v_mov_b32_e32 v41, v1
	v_mov_b32_e32 v42, v1
	v_mov_b32_e32 v43, v1
	v_mov_b32_e32 v48, v1
	v_mov_b32_e32 v49, v1
	v_mov_b32_e32 v50, v1
	v_mov_b32_e32 v51, v1
	v_mov_b32_e32 v60, v1
	v_mov_b32_e32 v61, v1
	v_mov_b32_e32 v62, v1
	v_mov_b32_e32 v63, v1
	v_mov_b32_e32 v68, v1
	v_mov_b32_e32 v69, v1
	v_mov_b32_e32 v70, v1
	v_mov_b32_e32 v71, v1
	v_mov_b32_e32 v28, v1
	v_mov_b32_e32 v29, v1
	v_mov_b32_e32 v30, v1
	v_mov_b32_e32 v31, v1
	v_mov_b32_e32 v36, v1
	v_mov_b32_e32 v37, v1
	v_mov_b32_e32 v38, v1
	v_mov_b32_e32 v39, v1
	v_mov_b32_e32 v44, v1
	v_mov_b32_e32 v45, v1
	v_mov_b32_e32 v46, v1
	v_mov_b32_e32 v47, v1
	v_mov_b32_e32 v52, v1
	v_mov_b32_e32 v53, v1
	v_mov_b32_e32 v54, v1
	v_mov_b32_e32 v55, v1
	v_mov_b32_e32 v56, v1
	v_mov_b32_e32 v57, v1
	v_mov_b32_e32 v58, v1
	v_mov_b32_e32 v59, v1
	v_mov_b32_e32 v64, v1
	v_mov_b32_e32 v65, v1
	v_mov_b32_e32 v66, v1
	v_mov_b32_e32 v67, v1
	v_mov_b32_e32 v72, v1
	v_mov_b32_e32 v73, v1
	v_mov_b32_e32 v74, v1
	v_mov_b32_e32 v75, v1
	v_mov_b32_e32 v76, v1
	v_mov_b32_e32 v77, v1
	v_mov_b32_e32 v78, v1
	v_mov_b32_e32 v79, v1
.LBB1_7:
	s_mov_b32 s15, s17
	v_add_u32_e32 v80, s15, v101
	ds_read_b128 v[92:95], v80 offset:16384
	ds_read_b128 v[96:99], v80 offset:17408
	ds_read_b128 v[108:111], v80 offset:18432
	ds_read_b128 v[112:115], v80 offset:19456
	ds_read_b128 v[116:119], v80 offset:32768
	ds_read_b128 v[120:123], v80 offset:33792
	ds_read_b128 v[124:127], v80 offset:34816
	ds_read_b128 v[128:131], v80 offset:35840
	s_lshl_b32 s17, s7, 7
	s_ashr_i32 s23, s17, 31
	s_add_u32 s20, s11, s17
	s_addc_u32 s21, s12, s23
	s_add_u32 s22, s4, s17
	s_addc_u32 s23, s5, s23
	s_add_i32 s17, s19, s14
	s_add_i32 m0, s17, 0x4000
	v_add_u32_e32 v80, s15, v91
	global_load_lds_dwordx4 v84, s[20:21]
	ds_read_b128 v[132:135], v80
	ds_read_b128 v[136:139], v80 offset:1024
	s_add_i32 m0, s17, 0x6000
	ds_read_b128 v[140:143], v80 offset:2048
	global_load_lds_dwordx4 v88, s[20:21]
	ds_read_b128 v[144:147], v80 offset:3072
	ds_read_b128 v[148:151], v80 offset:4096
	s_mov_b32 m0, s17
	ds_read_b128 v[152:155], v80 offset:5120
	global_load_lds_dwordx4 v82, s[22:23]
	ds_read_b128 v[156:159], v80 offset:6144
	ds_read_b128 v[160:163], v80 offset:7168
	s_waitcnt vmcnt(3) lgkmcnt(0)
	s_barrier
	s_setprio 1
	v_mfma_f32_16x16x32_f16 v[76:79], v[92:95], v[132:135], v[76:79]
	s_add_u32 s20, s20, 0x40000
	s_addc_u32 s21, s21, 0
	s_add_i32 m0, s17, 0x8000
	v_mfma_f32_16x16x32_f16 v[72:75], v[108:111], v[132:135], v[72:75]
	global_load_lds_dwordx4 v84, s[20:21]
	s_add_i32 m0, s17, 0xa000
	v_mfma_f32_16x16x32_f16 v[64:67], v[92:95], v[140:143], v[64:67]
	global_load_lds_dwordx4 v88, s[20:21]
	s_add_i32 m0, s17, 0x2000
	v_mfma_f32_16x16x32_f16 v[56:59], v[108:111], v[140:143], v[56:59]
	global_load_lds_dwordx4 v86, s[22:23]
	v_mfma_f32_16x16x32_f16 v[76:79], v[96:99], v[136:139], v[76:79]
	v_mfma_f32_16x16x32_f16 v[72:75], v[112:115], v[136:139], v[72:75]
	v_mfma_f32_16x16x32_f16 v[64:67], v[96:99], v[144:147], v[64:67]
	v_mfma_f32_16x16x32_f16 v[56:59], v[112:115], v[144:147], v[56:59]
	v_mfma_f32_16x16x32_f16 v[52:55], v[92:95], v[148:151], v[52:55]
	v_mfma_f32_16x16x32_f16 v[44:47], v[108:111], v[148:151], v[44:47]
	v_mfma_f32_16x16x32_f16 v[36:39], v[92:95], v[156:159], v[36:39]
	v_mfma_f32_16x16x32_f16 v[28:31], v[108:111], v[156:159], v[28:31]
	v_mfma_f32_16x16x32_f16 v[52:55], v[96:99], v[152:155], v[52:55]
	v_mfma_f32_16x16x32_f16 v[44:47], v[112:115], v[152:155], v[44:47]
	v_mfma_f32_16x16x32_f16 v[36:39], v[96:99], v[160:163], v[36:39]
	v_mfma_f32_16x16x32_f16 v[28:31], v[112:115], v[160:163], v[28:31]
	v_mfma_f32_16x16x32_f16 v[68:71], v[116:119], v[132:135], v[68:71]
	v_mfma_f32_16x16x32_f16 v[60:63], v[124:127], v[132:135], v[60:63]
	v_mfma_f32_16x16x32_f16 v[48:51], v[116:119], v[140:143], v[48:51]
	v_mfma_f32_16x16x32_f16 v[40:43], v[124:127], v[140:143], v[40:43]
	v_mfma_f32_16x16x32_f16 v[68:71], v[120:123], v[136:139], v[68:71]
	v_mfma_f32_16x16x32_f16 v[60:63], v[128:131], v[136:139], v[60:63]
	v_mfma_f32_16x16x32_f16 v[48:51], v[120:123], v[144:147], v[48:51]
	v_mfma_f32_16x16x32_f16 v[40:43], v[128:131], v[144:147], v[40:43]
	v_mfma_f32_16x16x32_f16 v[32:35], v[116:119], v[148:151], v[32:35]
	v_mfma_f32_16x16x32_f16 v[24:27], v[124:127], v[148:151], v[24:27]
	s_add_i32 s7, s7, 1
	s_cmp_lg_u32 s7, 16
	v_mfma_f32_16x16x32_f16 v[16:19], v[116:119], v[156:159], v[16:19]
	s_cselect_b32 s7, s7, 0
	v_mfma_f32_16x16x32_f16 v[0:3], v[124:127], v[156:159], v[0:3]
	s_add_i32 s13, s13, -1
	v_mfma_f32_16x16x32_f16 v[32:35], v[120:123], v[152:155], v[32:35]
	s_mov_b32 s17, s10
	v_mfma_f32_16x16x32_f16 v[24:27], v[128:131], v[152:155], v[24:27]
	s_mov_b32 s10, s14
	v_mfma_f32_16x16x32_f16 v[16:19], v[120:123], v[160:163], v[16:19]
	s_mov_b32 s14, s15
	v_mfma_f32_16x16x32_f16 v[0:3], v[128:131], v[160:163], v[0:3]
	s_cmp_lg_u32 s13, 0
	s_setprio 0
	s_barrier
	s_cbranch_scc1 .LBB1_7
	s_sub_u32 s0, s0, s8
	s_subb_u32 s1, s1, s9
	s_add_u32 s0, s8, s0
	s_addc_u32 s1, s9, s1
	s_lshl_b32 s3, s3, 6
	s_or_b32 s3, s3, s16
	s_lshl_b32 s4, s6, 1
	v_lshrrev_b32_e32 v86, 5, v106
	v_pk_add_f32 v[78:79], v[22:23], v[78:79]
	v_pk_add_f32 v[76:77], v[20:21], v[76:77]
	v_pk_add_f32 v[72:73], v[12:13], v[72:73]
	s_or_b32 s3, s3, s4
	s_lshl_b32 s2, s2, 6
	v_cvt_pk_f16_f32 v76, v76, v77
	v_cvt_pk_f16_f32 v77, v78, v79
	v_cvt_pk_f16_f32 v78, v72, v73
	v_or_b32_e32 v72, s3, v86
	s_or_b32 s2, s2, s16
	v_ashrrev_i32_e32 v73, 31, v72
	v_pk_add_f32 v[70:71], v[10:11], v[70:71]
	v_pk_add_f32 v[68:69], v[8:9], v[68:69]
	v_pk_add_f32 v[60:61], v[4:5], v[60:61]
	s_or_b32 s2, s2, s4
	v_lshlrev_b64 v[72:73], 12, v[72:73]
	v_cvt_pk_f16_f32 v68, v68, v69
	v_cvt_pk_f16_f32 v69, v70, v71
	v_cvt_pk_f16_f32 v70, v60, v61
	v_or_b32_e32 v60, s2, v86
	v_mov_b32_e32 v91, 0
	v_pk_add_f32 v[74:75], v[14:15], v[74:75]
	v_lshl_add_u64 v[72:73], s[0:1], 0, v[72:73]
	v_ashrrev_i32_e32 v61, 31, v60
	v_cvt_pk_f16_f32 v79, v74, v75
	v_lshl_add_u64 v[74:75], v[72:73], 0, v[90:91]
	v_lshlrev_b64 v[60:61], 12, v[60:61]
	v_lshl_or_b32 v84, v102, 6, v100
	v_mov_b32_e32 v85, v91
	global_store_dwordx4 v[74:75], v[76:79], off sc1
	v_lshl_add_u64 v[74:75], s[0:1], 0, v[60:61]
	v_pk_add_f32 v[50:51], v[10:11], v[50:51]
	v_pk_add_f32 v[48:49], v[8:9], v[48:49]
	v_pk_add_f32 v[42:43], v[6:7], v[42:43]
	v_pk_add_f32 v[40:41], v[4:5], v[40:41]
	v_pk_add_f32 v[62:63], v[6:7], v[62:63]
	v_cvt_pk_f16_f32 v48, v48, v49
	v_cvt_pk_f16_f32 v49, v50, v51
	v_cvt_pk_f16_f32 v50, v40, v41
	v_cvt_pk_f16_f32 v51, v42, v43
	v_lshl_add_u64 v[40:41], v[74:75], 0, v[84:85]
	v_cvt_pk_f16_f32 v71, v62, v63
	v_lshl_add_u64 v[60:61], v[74:75], 0, v[90:91]
	global_store_dwordx4 v[40:41], v[48:51], off sc1
	v_pk_add_f32 v[42:43], v[22:23], v[54:55]
	v_pk_add_f32 v[40:41], v[20:21], v[52:53]
	v_lshl_or_b32 v80, v103, 6, v100
	v_lshl_or_b32 v82, v104, 6, v100
	v_mov_b32_e32 v81, v91
	v_mov_b32_e32 v83, v91
	global_store_dwordx4 v[60:61], v[68:71], off sc1
	v_pk_add_f32 v[62:63], v[22:23], v[66:67]
	v_pk_add_f32 v[60:61], v[20:21], v[64:65]
	v_pk_add_f32 v[58:59], v[14:15], v[58:59]
	v_pk_add_f32 v[56:57], v[12:13], v[56:57]
	v_cvt_pk_f16_f32 v40, v40, v41
	v_cvt_pk_f16_f32 v41, v42, v43
	v_pk_add_f32 v[46:47], v[14:15], v[46:47]
	v_pk_add_f32 v[42:43], v[12:13], v[44:45]
	v_pk_add_f32 v[34:35], v[10:11], v[34:35]
	v_pk_add_f32 v[32:33], v[8:9], v[32:33]
	v_pk_add_f32 v[26:27], v[6:7], v[26:27]
	v_pk_add_f32 v[24:25], v[4:5], v[24:25]
	v_pk_add_f32 v[22:23], v[22:23], v[38:39]
	v_pk_add_f32 v[20:21], v[20:21], v[36:37]
	v_pk_add_f32 v[14:15], v[14:15], v[30:31]
	v_pk_add_f32 v[12:13], v[12:13], v[28:29]
	v_pk_add_f32 v[10:11], v[10:11], v[18:19]
	v_pk_add_f32 v[8:9], v[8:9], v[16:17]
	v_pk_add_f32 v[2:3], v[6:7], v[2:3]
	v_pk_add_f32 v[0:1], v[4:5], v[0:1]
	v_cvt_pk_f16_f32 v60, v60, v61
	v_cvt_pk_f16_f32 v61, v62, v63
	v_cvt_pk_f16_f32 v62, v56, v57
	v_cvt_pk_f16_f32 v63, v58, v59
	v_lshl_add_u64 v[56:57], v[72:73], 0, v[84:85]
	v_cvt_pk_f16_f32 v42, v42, v43
	v_cvt_pk_f16_f32 v43, v46, v47
	v_lshl_add_u64 v[44:45], v[72:73], 0, v[80:81]
	v_cvt_pk_f16_f32 v32, v32, v33
	v_cvt_pk_f16_f32 v33, v34, v35
	v_cvt_pk_f16_f32 v34, v24, v25
	v_cvt_pk_f16_f32 v35, v26, v27
	v_lshl_add_u64 v[24:25], v[74:75], 0, v[80:81]
	v_cvt_pk_f16_f32 v20, v20, v21
	v_cvt_pk_f16_f32 v21, v22, v23
	v_cvt_pk_f16_f32 v22, v12, v13
	v_cvt_pk_f16_f32 v23, v14, v15
	v_lshl_add_u64 v[12:13], v[72:73], 0, v[82:83]
	v_cvt_pk_f16_f32 v8, v8, v9
	v_cvt_pk_f16_f32 v9, v10, v11
	v_cvt_pk_f16_f32 v10, v0, v1
	v_cvt_pk_f16_f32 v11, v2, v3
	v_lshl_add_u64 v[0:1], v[74:75], 0, v[82:83]
	global_store_dwordx4 v[56:57], v[60:63], off sc1
	global_store_dwordx4 v[44:45], v[40:43], off sc1
	global_store_dwordx4 v[24:25], v[32:35], off sc1
	global_store_dwordx4 v[12:13], v[20:23], off sc1
	global_store_dwordx4 v[0:1], v[8:11], off sc1
	s_waitcnt vmcnt(0)
	s_cmpk_gt_u32 s18, 0xff
	s_cbranch_scc1 .LBB1_10
	s_barrier

.LBB2_3:
	s_mov_b32 s16, s15
	v_add_u32_e32 v116, s16, v87
	v_add_u32_e32 v148, s16, v0
	ds_read_b128 v[88:91], v116 offset:16384
	ds_read_b128 v[92:95], v116 offset:17408
	ds_read_b128 v[96:99], v116 offset:18432
	ds_read_b128 v[100:103], v116 offset:19456
	ds_read_b128 v[104:107], v116 offset:32768
	ds_read_b128 v[108:111], v116 offset:33792
	ds_read_b128 v[112:115], v116 offset:34816
	ds_read_b128 v[116:119], v116 offset:35840
	s_lshl_b32 s15, s7, 7
	s_ashr_i32 s17, s15, 31
	s_add_u32 s18, s4, s15
	s_addc_u32 s19, s5, s17
	s_add_u32 s20, s2, s15
	s_addc_u32 s21, s3, s17
	s_add_i32 s15, s6, s14
	s_add_i32 m0, s15, 0x4000
	ds_read_b128 v[120:123], v148
	global_load_lds_dwordx4 v82, s[18:19]
	ds_read_b128 v[124:127], v148 offset:1024
	s_add_i32 m0, s15, 0x6000
	ds_read_b128 v[128:131], v148 offset:2048
	global_load_lds_dwordx4 v84, s[18:19]
	ds_read_b128 v[132:135], v148 offset:3072
	ds_read_b128 v[136:139], v148 offset:4096
	s_mov_b32 m0, s15
	ds_read_b128 v[140:143], v148 offset:5120
	global_load_lds_dwordx4 v82, s[20:21]
	ds_read_b128 v[144:147], v148 offset:6144
	ds_read_b128 v[148:151], v148 offset:7168
	s_waitcnt vmcnt(3) lgkmcnt(0)
	s_barrier
	s_setprio 1
	v_mfma_f32_16x16x32_f16 v[18:21], v[88:91], v[120:123], v[18:21]
	s_add_u32 s18, s18, 0x40000
	s_addc_u32 s19, s19, 0
	s_add_i32 m0, s15, 0x8000
	v_mfma_f32_16x16x32_f16 v[70:73], v[96:99], v[120:123], v[70:73]
	global_load_lds_dwordx4 v82, s[18:19]
	s_add_i32 m0, s15, 0xa000
	v_mfma_f32_16x16x32_f16 v[58:61], v[88:91], v[128:131], v[58:61]
	global_load_lds_dwordx4 v84, s[18:19]
	s_add_i32 m0, s15, 0x2000
	v_mfma_f32_16x16x32_f16 v[54:57], v[96:99], v[128:131], v[54:57]
	global_load_lds_dwordx4 v84, s[20:21]
	v_mfma_f32_16x16x32_f16 v[18:21], v[92:95], v[124:127], v[18:21]
	v_mfma_f32_16x16x32_f16 v[70:73], v[100:103], v[124:127], v[70:73]
	v_mfma_f32_16x16x32_f16 v[58:61], v[92:95], v[132:135], v[58:61]
	v_mfma_f32_16x16x32_f16 v[54:57], v[100:103], v[132:135], v[54:57]
	v_mfma_f32_16x16x32_f16 v[42:45], v[88:91], v[136:139], v[42:45]
	v_mfma_f32_16x16x32_f16 v[38:41], v[96:99], v[136:139], v[38:41]
	v_mfma_f32_16x16x32_f16 v[26:29], v[88:91], v[144:147], v[26:29]
	v_mfma_f32_16x16x32_f16 v[22:25], v[96:99], v[144:147], v[22:25]
	v_mfma_f32_16x16x32_f16 v[42:45], v[92:95], v[140:143], v[42:45]
	v_mfma_f32_16x16x32_f16 v[38:41], v[100:103], v[140:143], v[38:41]
	v_mfma_f32_16x16x32_f16 v[26:29], v[92:95], v[148:151], v[26:29]
	v_mfma_f32_16x16x32_f16 v[22:25], v[100:103], v[148:151], v[22:25]
	v_mfma_f32_16x16x32_f16 v[78:81], v[104:107], v[120:123], v[78:81]
	v_mfma_f32_16x16x32_f16 v[74:77], v[112:115], v[120:123], v[74:77]
	v_mfma_f32_16x16x32_f16 v[66:69], v[104:107], v[128:131], v[66:69]
	v_mfma_f32_16x16x32_f16 v[62:65], v[112:115], v[128:131], v[62:65]
	v_mfma_f32_16x16x32_f16 v[78:81], v[108:111], v[124:127], v[78:81]
	v_mfma_f32_16x16x32_f16 v[74:77], v[116:119], v[124:127], v[74:77]
	v_mfma_f32_16x16x32_f16 v[66:69], v[108:111], v[132:135], v[66:69]
	v_mfma_f32_16x16x32_f16 v[62:65], v[116:119], v[132:135], v[62:65]
	v_mfma_f32_16x16x32_f16 v[50:53], v[104:107], v[136:139], v[50:53]
	v_mfma_f32_16x16x32_f16 v[46:49], v[112:115], v[136:139], v[46:49]
	s_add_i32 s7, s7, 1
	s_cmp_lg_u32 s7, 16
	v_mfma_f32_16x16x32_f16 v[34:37], v[104:107], v[144:147], v[34:37]
	s_cselect_b32 s7, s7, 0
	v_mfma_f32_16x16x32_f16 v[30:33], v[112:115], v[144:147], v[30:33]
	s_add_i32 s11, s11, -1
	v_mfma_f32_16x16x32_f16 v[50:53], v[108:111], v[140:143], v[50:53]
	s_mov_b32 s15, s13
	v_mfma_f32_16x16x32_f16 v[46:49], v[116:119], v[140:143], v[46:49]
	s_mov_b32 s13, s14
	v_mfma_f32_16x16x32_f16 v[34:37], v[108:111], v[148:151], v[34:37]
	s_mov_b32 s14, s16
	v_mfma_f32_16x16x32_f16 v[30:33], v[116:119], v[148:151], v[30:33]
	s_cmp_lg_u32 s11, 0
	s_setprio 0
	s_barrier
	s_cbranch_scc1 .LBB2_3
	v_lshl_add_u32 v0, s0, 7, v86
	v_or_b32_e32 v88, s10, v1
	v_ashrrev_i32_e32 v1, 31, v0
	v_lshlrev_b64 v[82:83], 12, v[0:1]
	v_or_b32_e32 v88, s1, v88
	v_lshl_add_u64 v[82:83], s[8:9], 0, v[82:83]
	v_lshlrev_b32_e32 v88, 2, v88
	v_mov_b32_e32 v89, 0
	v_or_b32_e32 v84, 16, v0
	v_lshl_add_u64 v[82:83], v[82:83], 0, v[88:89]
	v_pk_add_f32 v[20:21], v[16:17], v[20:21]
	v_pk_add_f32 v[18:19], v[14:15], v[18:19]
	v_ashrrev_i32_e32 v85, 31, v84
	global_store_dwordx4 v[82:83], v[18:21], off sc1
	v_lshlrev_b64 v[84:85], 12, v[84:85]
	v_lshl_add_u64 v[84:85], s[8:9], 0, v[84:85]
	v_pk_add_f32 v[20:21], v[12:13], v[72:73]
	v_pk_add_f32 v[18:19], v[10:11], v[70:71]
	global_store_dwordx4 v[82:83], v[18:21], off offset:64 sc1
	v_or_b32_e32 v86, 32, v0
	v_lshl_add_u64 v[84:85], v[84:85], 0, v[88:89]
	v_pk_add_f32 v[20:21], v[8:9], v[80:81]
	v_pk_add_f32 v[18:19], v[6:7], v[78:79]
	global_store_dwordx4 v[82:83], v[18:21], off offset:512 sc1
	v_ashrrev_i32_e32 v87, 31, v86
	v_lshlrev_b64 v[86:87], 12, v[86:87]
	v_pk_add_f32 v[20:21], v[4:5], v[76:77]
	v_pk_add_f32 v[18:19], v[2:3], v[74:75]
	global_store_dwordx4 v[82:83], v[18:21], off offset:576 sc1
	v_lshl_add_u64 v[86:87], s[8:9], 0, v[86:87]
	v_or_b32_e32 v0, 48, v0
	v_pk_add_f32 v[20:21], v[16:17], v[60:61]
	v_pk_add_f32 v[18:19], v[14:15], v[58:59]
	global_store_dwordx4 v[84:85], v[18:21], off sc1
	v_ashrrev_i32_e32 v1, 31, v0
	v_lshl_add_u64 v[86:87], v[86:87], 0, v[88:89]
	v_pk_add_f32 v[20:21], v[12:13], v[56:57]
	v_pk_add_f32 v[18:19], v[10:11], v[54:55]
	global_store_dwordx4 v[84:85], v[18:21], off offset:64 sc1
	v_lshlrev_b64 v[0:1], 12, v[0:1]
	v_lshl_add_u64 v[0:1], s[8:9], 0, v[0:1]
	v_pk_add_f32 v[20:21], v[8:9], v[68:69]
	v_pk_add_f32 v[18:19], v[6:7], v[66:67]
	global_store_dwordx4 v[84:85], v[18:21], off offset:512 sc1
	v_lshl_add_u64 v[0:1], v[0:1], 0, v[88:89]
	s_cmpk_gt_u32 s12, 0xff
	v_pk_add_f32 v[20:21], v[4:5], v[64:65]
	v_pk_add_f32 v[18:19], v[2:3], v[62:63]
	global_store_dwordx4 v[84:85], v[18:21], off offset:576 sc1
	s_nop 1
	v_pk_add_f32 v[20:21], v[16:17], v[44:45]
	v_pk_add_f32 v[18:19], v[14:15], v[42:43]
	global_store_dwordx4 v[86:87], v[18:21], off sc1
	v_pk_add_f32 v[16:17], v[16:17], v[28:29]
	v_pk_add_f32 v[14:15], v[14:15], v[26:27]
	v_pk_add_f32 v[20:21], v[12:13], v[40:41]
	v_pk_add_f32 v[18:19], v[10:11], v[38:39]
	global_store_dwordx4 v[86:87], v[18:21], off offset:64 sc1
	v_pk_add_f32 v[12:13], v[12:13], v[24:25]
	v_pk_add_f32 v[10:11], v[10:11], v[22:23]
	v_pk_add_f32 v[20:21], v[8:9], v[52:53]
	v_pk_add_f32 v[18:19], v[6:7], v[50:51]
	global_store_dwordx4 v[86:87], v[18:21], off offset:512 sc1
	v_pk_add_f32 v[8:9], v[8:9], v[36:37]
	v_pk_add_f32 v[6:7], v[6:7], v[34:35]
	v_pk_add_f32 v[20:21], v[4:5], v[48:49]
	v_pk_add_f32 v[18:19], v[2:3], v[46:47]
	v_pk_add_f32 v[4:5], v[4:5], v[32:33]
	v_pk_add_f32 v[2:3], v[2:3], v[30:31]
	global_store_dwordx4 v[86:87], v[18:21], off offset:576 sc1
	global_store_dwordx4 v[0:1], v[14:17], off sc1
	global_store_dwordx4 v[0:1], v[10:13], off offset:64 sc1
	global_store_dwordx4 v[0:1], v[6:9], off offset:512 sc1
	global_store_dwordx4 v[0:1], v[2:5], off offset:576 sc1
	s_waitcnt vmcnt(0)
	s_cbranch_scc1 .LBB2_6
	s_barrier
